# flag barrier polls without the s_sleep between polls (on the split barrier-1 version)
# baseline (speedup 1.0000x reference)
; __device__ __forceinline__ unsigned xb_ld(unsigned* p)              { return __hip_atomic_load(p, __ATOMIC_RELAXED, __HIP_MEMORY_SCOPE_AGENT); }
; #define XB_SPIN(cond, bar) do { unsigned _sp = 0; while (cond) { __builtin_amdgcn_s_sleep(1); \
;     if ((++_sp & 255u) == 0u) { if (xb_ld(&(bar)[XB_TMO])) break; if (_sp > XB_SPIN_CAP) { atomicAdd(&(bar)[XB_TMO], 1u); break; } } } } while (0)
; __device__ __forceinline__ void xcd_barrier(const XcdBarrier& b, const int wave) {
;     ...
;             else XB_SPIN(xb_ld(&bar[XB_TOPGEN]) == tg, bar);
;             __builtin_amdgcn_fence(__ATOMIC_ACQUIRE, "agent");
.Lmy_gb1_poll:
	global_load_dwordx4 v[2:5], v0, s[30:31] sc1
	global_load_dwordx4 v[6:9], v0, s[30:31] offset:16 sc1
	s_waitcnt vmcnt(0)
	v_min_u32_e32 v2, v2, v3
	v_min_u32_e32 v4, v4, v5
	v_min_u32_e32 v6, v6, v7
	v_min_u32_e32 v8, v8, v9
	v_min_u32_e32 v2, v2, v4
	v_min_u32_e32 v6, v6, v8
	v_min_u32_e32 v1, v2, v6
	v_cmp_gt_u32_e32 vcc, 1, v1
	s_cbranch_vccz .Lmy_gb1_done
	s_add_u32 s2, s2, 1
	s_cmp_lt_u32 s2, 0x40000
	s_cbranch_scc1 .Lmy_gb1_poll

; __device__ __forceinline__ unsigned xb_ld(unsigned* p)              { return __hip_atomic_load(p, __ATOMIC_RELAXED, __HIP_MEMORY_SCOPE_AGENT); }
; #define XB_SPIN(cond, bar) do { unsigned _sp = 0; while (cond) { __builtin_amdgcn_s_sleep(1); \
;     if ((++_sp & 255u) == 0u) { if (xb_ld(&(bar)[XB_TMO])) break; if (_sp > XB_SPIN_CAP) { atomicAdd(&(bar)[XB_TMO], 1u); break; } } } } while (0)
; __device__ __forceinline__ void xcd_barrier(const XcdBarrier& b, const int wave) {
;     ...
;             else XB_SPIN(xb_ld(&bar[XB_TOPGEN]) == tg, bar);
;             __builtin_amdgcn_fence(__ATOMIC_ACQUIRE, "agent");
.Lmy_gb2_poll:
	global_load_dwordx4 v[2:5], v0, s[30:31] sc1
	global_load_dwordx4 v[6:9], v0, s[30:31] offset:16 sc1
	s_waitcnt vmcnt(0)
	v_min_u32_e32 v2, v2, v3
	v_min_u32_e32 v4, v4, v5
	v_min_u32_e32 v6, v6, v7
	v_min_u32_e32 v8, v8, v9
	v_min_u32_e32 v2, v2, v4
	v_min_u32_e32 v6, v6, v8
	v_min_u32_e32 v1, v2, v6
	v_cmp_gt_u32_e32 vcc, 2, v1
	s_cbranch_vccz .Lmy_gb2_done
	s_add_u32 s2, s2, 1
	s_cmp_lt_u32 s2, 0x40000
	s_cbranch_scc1 .Lmy_gb2_poll

; __device__ __forceinline__ unsigned xb_ld(unsigned* p)              { return __hip_atomic_load(p, __ATOMIC_RELAXED, __HIP_MEMORY_SCOPE_AGENT); }
; #define XB_SPIN(cond, bar) do { unsigned _sp = 0; while (cond) { __builtin_amdgcn_s_sleep(1); \
;     if ((++_sp & 255u) == 0u) { if (xb_ld(&(bar)[XB_TMO])) break; if (_sp > XB_SPIN_CAP) { atomicAdd(&(bar)[XB_TMO], 1u); break; } } } } while (0)
; __device__ __forceinline__ void xcd_barrier(const XcdBarrier& b, const int wave) {
;     ...
;             else XB_SPIN(xb_ld(&bar[XB_TOPGEN]) == tg, bar);
;             __builtin_amdgcn_fence(__ATOMIC_ACQUIRE, "agent");
.Lmy_gb3_poll:
	global_load_dwordx4 v[2:5], v0, s[30:31] sc1
	global_load_dwordx4 v[6:9], v0, s[30:31] offset:16 sc1
	s_waitcnt vmcnt(0)
	v_min_u32_e32 v2, v2, v3
	v_min_u32_e32 v4, v4, v5
	v_min_u32_e32 v6, v6, v7
	v_min_u32_e32 v8, v8, v9
	v_min_u32_e32 v2, v2, v4
	v_min_u32_e32 v6, v6, v8
	v_min_u32_e32 v1, v2, v6
	v_cmp_gt_u32_e32 vcc, 3, v1
	s_cbranch_vccz .Lmy_gb3_done
	s_add_u32 s2, s2, 1
	s_cmp_lt_u32 s2, 0x40000
	s_cbranch_scc1 .Lmy_gb3_poll

; __device__ __forceinline__ unsigned xb_ld(unsigned* p)              { return __hip_atomic_load(p, __ATOMIC_RELAXED, __HIP_MEMORY_SCOPE_AGENT); }
; #define XB_SPIN(cond, bar) do { unsigned _sp = 0; while (cond) { __builtin_amdgcn_s_sleep(1); \
;     if ((++_sp & 255u) == 0u) { if (xb_ld(&(bar)[XB_TMO])) break; if (_sp > XB_SPIN_CAP) { atomicAdd(&(bar)[XB_TMO], 1u); break; } } } } while (0)
; __device__ __forceinline__ void xcd_barrier(const XcdBarrier& b, const int wave) {
;     ...
;             else XB_SPIN(xb_ld(&bar[XB_TOPGEN]) == tg, bar);
;             __builtin_amdgcn_fence(__ATOMIC_ACQUIRE, "agent");
.Lmy_gb4_poll:
	global_load_dwordx4 v[2:5], v0, s[30:31] sc1
	global_load_dwordx4 v[6:9], v0, s[30:31] offset:16 sc1
	s_waitcnt vmcnt(0)
	v_min_u32_e32 v2, v2, v3
	v_min_u32_e32 v4, v4, v5
	v_min_u32_e32 v6, v6, v7
	v_min_u32_e32 v8, v8, v9
	v_min_u32_e32 v2, v2, v4
	v_min_u32_e32 v6, v6, v8
	v_min_u32_e32 v1, v2, v6
	v_cmp_gt_u32_e32 vcc, 4, v1
	s_cbranch_vccz .Lmy_gb4_done
	s_add_u32 s2, s2, 1
	s_cmp_lt_u32 s2, 0x40000
	s_cbranch_scc1 .Lmy_gb4_poll

; __device__ __forceinline__ unsigned xb_ld(unsigned* p)              { return __hip_atomic_load(p, __ATOMIC_RELAXED, __HIP_MEMORY_SCOPE_AGENT); }
; #define XB_SPIN(cond, bar) do { unsigned _sp = 0; while (cond) { __builtin_amdgcn_s_sleep(1); \
;     if ((++_sp & 255u) == 0u) { if (xb_ld(&(bar)[XB_TMO])) break; if (_sp > XB_SPIN_CAP) { atomicAdd(&(bar)[XB_TMO], 1u); break; } } } } while (0)
; __device__ __forceinline__ void xcd_barrier(const XcdBarrier& b, const int wave) {
;     ...
;             else XB_SPIN(xb_ld(&bar[XB_TOPGEN]) == tg, bar);
;             __builtin_amdgcn_fence(__ATOMIC_ACQUIRE, "agent");
.Lmy_gb5_poll:
	global_load_dwordx4 v[2:5], v0, s[30:31] sc1
	global_load_dwordx4 v[6:9], v0, s[30:31] offset:16 sc1
	s_waitcnt vmcnt(0)
	v_min_u32_e32 v2, v2, v3
	v_min_u32_e32 v4, v4, v5
	v_min_u32_e32 v6, v6, v7
	v_min_u32_e32 v8, v8, v9
	v_min_u32_e32 v2, v2, v4
	v_min_u32_e32 v6, v6, v8
	v_min_u32_e32 v1, v2, v6
	v_cmp_gt_u32_e32 vcc, 5, v1
	s_cbranch_vccz .Lmy_gb5_done
	s_add_u32 s2, s2, 1
	s_cmp_lt_u32 s2, 0x40000
	s_cbranch_scc1 .Lmy_gb5_poll

; __device__ __forceinline__ unsigned xb_ld(unsigned* p)              { return __hip_atomic_load(p, __ATOMIC_RELAXED, __HIP_MEMORY_SCOPE_AGENT); }
; #define XB_SPIN(cond, bar) do { unsigned _sp = 0; while (cond) { __builtin_amdgcn_s_sleep(1); \
;     if ((++_sp & 255u) == 0u) { if (xb_ld(&(bar)[XB_TMO])) break; if (_sp > XB_SPIN_CAP) { atomicAdd(&(bar)[XB_TMO], 1u); break; } } } } while (0)
; __device__ __forceinline__ void xcd_barrier(const XcdBarrier& b, const int wave) {
;     ...
;             else XB_SPIN(xb_ld(&bar[XB_TOPGEN]) == tg, bar);
;             __builtin_amdgcn_fence(__ATOMIC_ACQUIRE, "agent");
.Lmy_gb6_poll:
	global_load_dwordx4 v[2:5], v0, s[30:31] sc1
	global_load_dwordx4 v[6:9], v0, s[30:31] offset:16 sc1
	s_waitcnt vmcnt(0)
	v_min_u32_e32 v2, v2, v3
	v_min_u32_e32 v4, v4, v5
	v_min_u32_e32 v6, v6, v7
	v_min_u32_e32 v8, v8, v9
	v_min_u32_e32 v2, v2, v4
	v_min_u32_e32 v6, v6, v8
	v_min_u32_e32 v1, v2, v6
	v_cmp_gt_u32_e32 vcc, 6, v1
	s_cbranch_vccz .Lmy_gb6_done
	s_add_u32 s2, s2, 1
	s_cmp_lt_u32 s2, 0x40000
	s_cbranch_scc1 .Lmy_gb6_poll

; __device__ __forceinline__ unsigned xb_ld(unsigned* p)              { return __hip_atomic_load(p, __ATOMIC_RELAXED, __HIP_MEMORY_SCOPE_AGENT); }
; #define XB_SPIN(cond, bar) do { unsigned _sp = 0; while (cond) { __builtin_amdgcn_s_sleep(1); \
;     if ((++_sp & 255u) == 0u) { if (xb_ld(&(bar)[XB_TMO])) break; if (_sp > XB_SPIN_CAP) { atomicAdd(&(bar)[XB_TMO], 1u); break; } } } } while (0)
; __device__ __forceinline__ void xcd_barrier(const XcdBarrier& b, const int wave) {
;     ...
;             else XB_SPIN(xb_ld(&bar[XB_TOPGEN]) == tg, bar);
;             __builtin_amdgcn_fence(__ATOMIC_ACQUIRE, "agent");
.Lmy_gb7_poll:
	global_load_dwordx4 v[2:5], v0, s[30:31] sc1
	global_load_dwordx4 v[6:9], v0, s[30:31] offset:16 sc1
	s_waitcnt vmcnt(0)
	v_min_u32_e32 v2, v2, v3
	v_min_u32_e32 v4, v4, v5
	v_min_u32_e32 v6, v6, v7
	v_min_u32_e32 v8, v8, v9
	v_min_u32_e32 v2, v2, v4
	v_min_u32_e32 v6, v6, v8
	v_min_u32_e32 v1, v2, v6
	v_cmp_gt_u32_e32 vcc, 7, v1
	s_cbranch_vccz .Lmy_gb7_done
	s_add_u32 s2, s2, 1
	s_cmp_lt_u32 s2, 0x40000
	s_cbranch_scc1 .Lmy_gb7_poll

; __device__ __forceinline__ unsigned xb_ld(unsigned* p)              { return __hip_atomic_load(p, __ATOMIC_RELAXED, __HIP_MEMORY_SCOPE_AGENT); }
; #define XB_SPIN(cond, bar) do { unsigned _sp = 0; while (cond) { __builtin_amdgcn_s_sleep(1); \
;     if ((++_sp & 255u) == 0u) { if (xb_ld(&(bar)[XB_TMO])) break; if (_sp > XB_SPIN_CAP) { atomicAdd(&(bar)[XB_TMO], 1u); break; } } } } while (0)
; __device__ __forceinline__ void xcd_barrier(const XcdBarrier& b, const int wave) {
;     ...
;             else XB_SPIN(xb_ld(&bar[XB_TOPGEN]) == tg, bar);
;             __builtin_amdgcn_fence(__ATOMIC_ACQUIRE, "agent");
.Lmy_gb8_poll:
	global_load_dwordx4 v[2:5], v0, s[30:31] sc1
	global_load_dwordx4 v[6:9], v0, s[30:31] offset:16 sc1
	s_waitcnt vmcnt(0)
	v_min_u32_e32 v2, v2, v3
	v_min_u32_e32 v4, v4, v5
	v_min_u32_e32 v6, v6, v7
	v_min_u32_e32 v8, v8, v9
	v_min_u32_e32 v2, v2, v4
	v_min_u32_e32 v6, v6, v8
	v_min_u32_e32 v1, v2, v6
	v_cmp_gt_u32_e32 vcc, 8, v1
	s_cbranch_vccz .Lmy_gb8_done
	s_add_u32 s2, s2, 1
	s_cmp_lt_u32 s2, 0x40000
	s_cbranch_scc1 .Lmy_gb8_poll

; __device__ __forceinline__ unsigned xb_ld(unsigned* p)              { return __hip_atomic_load(p, __ATOMIC_RELAXED, __HIP_MEMORY_SCOPE_AGENT); }
; __device__ __forceinline__ unsigned xb_add(unsigned* p, unsigned v) { return __hip_atomic_fetch_add(p, v, __ATOMIC_RELAXED, __HIP_MEMORY_SCOPE_AGENT); }
; #define XB_SPIN(cond, bar) do { unsigned _sp = 0; while (cond) { __builtin_amdgcn_s_sleep(1); \
;     if ((++_sp & 255u) == 0u) { if (xb_ld(&(bar)[XB_TMO])) break; if (_sp > XB_SPIN_CAP) { atomicAdd(&(bar)[XB_TMO], 1u); break; } } } } while (0)
; __device__ __forceinline__ void xcd_barrier(const XcdBarrier& b, const int wave) {
;     ...
;             else XB_SPIN(xb_ld(&bar[XB_TOPGEN]) == tg, bar);
;             __builtin_amdgcn_fence(__ATOMIC_ACQUIRE, "agent");
;             xb_add(&bar[XB_XGEN(b.x)], 1u);
;             asm volatile("s_waitcnt vmcnt(0)" ::: "memory");
;         } else {
;             XB_SPIN(xb_ld(&bar[XB_XGEN(b.x)]) == gen, bar);
.Lmy_gb9_poll:
	global_load_dwordx4 v[2:5], v0, s[30:31] sc1
	global_load_dwordx4 v[6:9], v0, s[30:31] offset:16 sc1
	s_waitcnt vmcnt(0)
	v_min_u32_e32 v2, v2, v3
	v_min_u32_e32 v4, v4, v5
	v_min_u32_e32 v6, v6, v7
	v_min_u32_e32 v8, v8, v9
	v_min_u32_e32 v2, v2, v4
	v_min_u32_e32 v6, v6, v8
	v_min_u32_e32 v1, v2, v6
	v_cmp_gt_u32_e32 vcc, 9, v1
	s_cbranch_vccz .Lmy_gb9_done
	s_add_u32 s2, s2, 1
	s_cmp_lt_u32 s2, 0x40000
	s_cbranch_scc1 .Lmy_gb9_poll

; __device__ __forceinline__ unsigned xb_ld(unsigned* p)              { return __hip_atomic_load(p, __ATOMIC_RELAXED, __HIP_MEMORY_SCOPE_AGENT); }
; __device__ __forceinline__ unsigned xb_add(unsigned* p, unsigned v) { return __hip_atomic_fetch_add(p, v, __ATOMIC_RELAXED, __HIP_MEMORY_SCOPE_AGENT); }
; #define XB_SPIN(cond, bar) do { unsigned _sp = 0; while (cond) { __builtin_amdgcn_s_sleep(1); \
;     if ((++_sp & 255u) == 0u) { if (xb_ld(&(bar)[XB_TMO])) break; if (_sp > XB_SPIN_CAP) { atomicAdd(&(bar)[XB_TMO], 1u); break; } } } } while (0)
; __device__ __forceinline__ void xcd_barrier(const XcdBarrier& b, const int wave) {
;     ...
;             else XB_SPIN(xb_ld(&bar[XB_TOPGEN]) == tg, bar);
;             __builtin_amdgcn_fence(__ATOMIC_ACQUIRE, "agent");
;             xb_add(&bar[XB_XGEN(b.x)], 1u);
;             asm volatile("s_waitcnt vmcnt(0)" ::: "memory");
;         } else {
;             XB_SPIN(xb_ld(&bar[XB_XGEN(b.x)]) == gen, bar);
.Lmy_gb10_poll:
	global_load_dwordx4 v[2:5], v0, s[30:31] sc1
	global_load_dwordx4 v[6:9], v0, s[30:31] offset:16 sc1
	s_waitcnt vmcnt(0)
	v_min_u32_e32 v2, v2, v3
	v_min_u32_e32 v4, v4, v5
	v_min_u32_e32 v6, v6, v7
	v_min_u32_e32 v8, v8, v9
	v_min_u32_e32 v2, v2, v4
	v_min_u32_e32 v6, v6, v8
	v_min_u32_e32 v1, v2, v6
	v_cmp_gt_u32_e32 vcc, 10, v1
	s_cbranch_vccz .Lmy_gb10_done
	s_add_u32 s2, s2, 1
	s_cmp_lt_u32 s2, 0x40000
	s_cbranch_scc1 .Lmy_gb10_poll

; __device__ __forceinline__ unsigned xb_ld(unsigned* p)              { return __hip_atomic_load(p, __ATOMIC_RELAXED, __HIP_MEMORY_SCOPE_AGENT); }
; __device__ __forceinline__ unsigned xb_add(unsigned* p, unsigned v) { return __hip_atomic_fetch_add(p, v, __ATOMIC_RELAXED, __HIP_MEMORY_SCOPE_AGENT); }
; #define XB_SPIN(cond, bar) do { unsigned _sp = 0; while (cond) { __builtin_amdgcn_s_sleep(1); \
;     if ((++_sp & 255u) == 0u) { if (xb_ld(&(bar)[XB_TMO])) break; if (_sp > XB_SPIN_CAP) { atomicAdd(&(bar)[XB_TMO], 1u); break; } } } } while (0)
; __device__ __forceinline__ void xcd_barrier(const XcdBarrier& b, const int wave) {
;     ...
;             else XB_SPIN(xb_ld(&bar[XB_TOPGEN]) == tg, bar);
;             __builtin_amdgcn_fence(__ATOMIC_ACQUIRE, "agent");
;             xb_add(&bar[XB_XGEN(b.x)], 1u);
;             asm volatile("s_waitcnt vmcnt(0)" ::: "memory");
;         } else {
;             XB_SPIN(xb_ld(&bar[XB_XGEN(b.x)]) == gen, bar);
.Lmy_gb11_poll:
	global_load_dwordx4 v[2:5], v0, s[30:31] sc1
	global_load_dwordx4 v[6:9], v0, s[30:31] offset:16 sc1
	s_waitcnt vmcnt(0)
	v_min_u32_e32 v2, v2, v3
	v_min_u32_e32 v4, v4, v5
	v_min_u32_e32 v6, v6, v7
	v_min_u32_e32 v8, v8, v9
	v_min_u32_e32 v2, v2, v4
	v_min_u32_e32 v6, v6, v8
	v_min_u32_e32 v1, v2, v6
	v_cmp_gt_u32_e32 vcc, 11, v1
	s_cbranch_vccz .Lmy_gb11_done
	s_add_u32 s2, s2, 1
	s_cmp_lt_u32 s2, 0x40000
	s_cbranch_scc1 .Lmy_gb11_poll
